# speedup vs baseline: 1.0072x; 1.0072x over previous
.Lstag_done_p1:
	s_lshr_b32 s22, s2, 3
	s_sub_i32 s22, 0xbf, s22
	s_and_b32 s2, s2, 7
	s_lshl_b32 s22, s22, 3
	s_or_b32 s2, s2, s22
	s_ashr_i32 s15, s2, 3
	s_mul_hi_i32 s14, s15, 0x55555556
	s_lshr_b32 s12, s14, 31
	s_add_i32 s14, s14, s12
	s_mul_i32 s16, s14, 0x3fffffd
	s_add_i32 s16, s16, s15
	s_lshl_b32 s15, s16, 6
	s_lshl_b32 s16, s2, 5
	s_and_b32 s16, s16, 32
	s_or_b32 s15, s15, s16
	s_bfe_u32 s16, s2, 0x20001
	s_mul_i32 s2, s16, 0xc0
	s_lshl_b32 s12, s14, 1
	s_add_i32 s17, s15, s2
	s_load_dwordx8 s[4:11], s[0:1], 0x0
	s_and_b32 s12, s12, -16
	s_lshl_b32 s13, s14, 4
	s_and_b32 s13, s13, 0x70
	s_mov_b32 s3, 0
	v_mov_b32_e32 v32, 0
	v_lshrrev_b32_e32 v78, 6, v0
	v_bfe_u32 v65, v0, 2, 4
	v_lshlrev_b32_e32 v1, 4, v0
	v_and_b32_e32 v30, 48, v1
	v_lshl_add_u32 v1, v78, 7, v65
	v_lshl_add_u32 v1, v1, 9, v30
	s_lshl_b32 s18, s17, 7
	s_add_i32 s18, s18, s12
	s_lshl_b32 s18, s18, 9
	s_lshl_b32 s2, s13, 2
	s_add_i32 s18, s18, s2
	s_waitcnt lgkmcnt(0)
	s_add_u32 s20, s4, s18
	s_addc_u32 s21, s5, 0
	s_add_u32 s22, s20, 0x40000
	s_addc_u32 s23, s21, 0
	s_add_u32 s24, s22, 0x40000
	s_addc_u32 s25, s23, 0
	s_add_u32 s26, s24, 0x40000
	s_addc_u32 s27, s25, 0
	s_add_u32 s28, s26, 0x40000
	s_addc_u32 s29, s27, 0
	s_add_u32 s30, s28, 0x40000
	s_addc_u32 s31, s29, 0
	s_add_u32 s32, s30, 0x40000
	s_addc_u32 s33, s31, 0
	s_add_u32 s34, s32, 0x40000
	s_addc_u32 s35, s33, 0
	global_load_dwordx4 v[2:5], v1, s[34:35]
	global_load_dwordx4 v[6:9], v1, s[32:33]
	global_load_dwordx4 v[10:13], v1, s[30:31]
	global_load_dwordx4 v[14:17], v1, s[28:29]
	global_load_dwordx4 v[18:21], v1, s[26:27]
	global_load_dwordx4 v[22:25], v1, s[24:25]
	v_bfe_u32 v103, v0, 5, 1
	v_lshrrev_b32_e32 v33, 2, v0
	global_load_dwordx4 v[66:69], v1, s[22:23]
	global_load_dwordx4 v[74:77], v1, s[20:21]
	v_lshlrev_b32_e32 v104, 1, v78
	v_and_b32_e32 v27, 3, v0
	v_lshrrev_b32_e32 v28, 1, v0
	v_and_or_b32 v59, v33, 1, v104
	v_and_or_b32 v105, v28, 12, v27
	v_lshlrev_b32_e32 v28, 4, v103
	v_mov_b32_e32 v29, v32
	v_lshl_add_u64 v[56:57], s[6:7], 0, v[28:29]
	v_or_b32_e32 v27, s13, v59
	v_or_b32_e32 v28, s12, v105
	s_lshl_b32 s4, s16, 16
	v_lshl_add_u32 v31, v27, 7, v28
	s_or_b32 s2, s4, 0x4000
	v_add_u32_e32 v27, 0x400, v31
	s_or_b32 s5, s4, 0xc000
	v_add_u32_e32 v28, s2, v27
	v_and_b32_e32 v1, 31, v0
	v_ashrrev_i32_e32 v29, 31, v28
	v_add_u32_e32 v34, s5, v27
	v_or_b32_e32 v26, s15, v1
	v_lshlrev_b64 v[28:29], 5, v[28:29]
	v_ashrrev_i32_e32 v35, 31, v34
	v_lshl_add_u64 v[28:29], v[56:57], 0, v[28:29]
	v_lshlrev_b64 v[34:35], 5, v[34:35]
	v_lshl_or_b32 v58, v26, 1, v103
	v_lshl_add_u64 v[34:35], v[56:57], 0, v[34:35]
	global_load_dwordx4 v[36:39], v[28:29], off
	global_load_dwordx4 v[40:43], v[34:35], off
	v_add_u32_e32 v28, 0x180, v58
	v_ashrrev_i32_e32 v29, 31, v28
	v_add_u32_e32 v34, 0x480, v58
	v_lshl_add_u64 v[28:29], v[28:29], 4, s[8:9]
	v_ashrrev_i32_e32 v35, 31, v34
	v_ashrrev_i32_e32 v27, 31, v26
	v_lshl_add_u64 v[34:35], v[34:35], 4, s[8:9]
	global_load_dwordx4 v[44:47], v[28:29], off
	global_load_dwordx4 v[48:51], v[34:35], off
	v_lshl_add_u64 v[60:61], v[26:27], 2, s[10:11]
	v_add_u32_e32 v26, s5, v31
	v_add_u32_e32 v28, s2, v31
	v_ashrrev_i32_e32 v27, 31, v26
	v_ashrrev_i32_e32 v29, 31, v28
	v_lshlrev_b64 v[26:27], 5, v[26:27]
	v_lshlrev_b64 v[28:29], 5, v[28:29]
	global_load_dword v62, v[60:61], off offset:768
	global_load_dword v64, v[60:61], off offset:2304
	v_lshl_add_u64 v[26:27], v[56:57], 0, v[26:27]
	v_lshl_add_u64 v[28:29], v[56:57], 0, v[28:29]
	global_load_dwordx4 v[52:55], v[26:27], off
	s_nop 0
	global_load_dwordx4 v[26:29], v[28:29], off
	v_add_u32_e32 v120, s12, v59
	v_or_b32_e32 v121, s13, v105
	v_lshl_or_b32 v120, v120, 7, v121
	s_or_b32 s18, s4, 0x8000
	v_add_u32_e32 v122, s18, v120
	v_add_u32_e32 v124, s4, v120
	v_ashrrev_i32_e32 v123, 31, v122
	v_ashrrev_i32_e32 v125, 31, v124
	v_lshlrev_b64 v[122:123], 5, v[122:123]
	v_lshlrev_b64 v[124:125], 5, v[124:125]
	v_lshl_add_u64 v[122:123], v[56:57], 0, v[122:123]
	v_lshl_add_u64 v[124:125], v[56:57], 0, v[124:125]
	v_mov_b32_e32 v110, v58
	v_ashrrev_i32_e32 v111, 31, v58
	v_lshl_add_u64 v[112:113], v[110:111], 4, s[8:9]
	v_add_u32_e32 v114, 0x300, v58
	v_ashrrev_i32_e32 v115, 31, v114
	v_lshl_add_u64 v[114:115], v[114:115], 4, s[8:9]
	global_load_dwordx4 v[110:113], v[112:113], off
	global_load_dwordx4 v[114:117], v[114:115], off
	global_load_dword v118, v[60:61], off
	global_load_dword v119, v[60:61], off offset:1536
	global_load_dwordx4 v[120:123], v[122:123], off
	global_load_dwordx4 v[124:127], v[124:125], off
	s_load_dwordx2 s[0:1], s[0:1], 0x28
	v_and_b32_e32 v0, 63, v0
	v_bfrev_b32_e32 v31, 60
	v_cmp_gt_u32_e32 vcc, 32, v0
	v_mul_u32_u24_e32 v102, 0x410, v1
	v_lshlrev_b32_e32 v0, 2, v1
	v_mov_b32_e32 v1, v32
	v_cndmask_b32_e64 v34, v31, 0, vcc
	s_waitcnt lgkmcnt(0)
	v_lshl_add_u64 v[72:73], s[0:1], 0, v[0:1]
	v_mul_u32_u24_e32 v0, 0x410, v78
	v_lshlrev_b32_e32 v1, 6, v65
	v_add3_u32 v1, v0, v1, v30
	s_mul_i32 s16, s16, 24
	s_lshr_b32 s0, s15, 5
	s_waitcnt vmcnt(14)
	ds_write_b128 v1, v[74:77]
	ds_write_b128 v1, v[66:69] offset:4160
	ds_write_b128 v1, v[22:25] offset:8320
	ds_write_b128 v1, v[18:21] offset:12480
	ds_write_b128 v1, v[14:17] offset:16640
	ds_write_b128 v1, v[10:13] offset:20800
	ds_write_b128 v1, v[6:9] offset:24960
	ds_write_b128 v1, v[2:5] offset:29120
	s_add_i32 s0, s0, s16
	s_waitcnt lgkmcnt(0)
	s_barrier
	s_lshl_b32 s2, s0, 10
	v_mov_b32_e32 v33, v32
	v_mov_b32_e32 v35, v32
	v_lshl_or_b32 v106, v103, 2, v102
	s_add_i32 s5, s2, 0x4800
	v_or_b32_e32 v107, s13, v103
	s_ashr_i32 s6, s14, 3
	s_add_i32 s7, s2, 0x1800
	s_mov_b64 s[0:1], -1
	s_mov_b32 s10, 0x7f61b1e6
	s_mov_b32 s11, 0x42800000
	s_waitcnt vmcnt(9)
	v_mov_b32_e32 v63, v62
	s_waitcnt vmcnt(8)
	v_mov_b32_e32 v65, v64
	s_waitcnt vmcnt(6)
	s_branch .LBB2_3

.LBB2_8:
	v_add_u32_e32 v0, s12, v59
	v_or_b32_e32 v1, s13, v105
	v_lshl_or_b32 v4, v0, 7, v1
	s_or_b32 s0, s4, 0x8000
	v_add_u32_e32 v2, 0x400, v4
	v_add_u32_e32 v0, s4, v2
	v_add_u32_e32 v2, s0, v2
	v_ashrrev_i32_e32 v1, 31, v0
	v_ashrrev_i32_e32 v3, 31, v2
	v_lshlrev_b64 v[0:1], 5, v[0:1]
	v_lshlrev_b64 v[2:3], 5, v[2:3]
	v_lshl_add_u64 v[0:1], v[56:57], 0, v[0:1]
	v_lshl_add_u64 v[2:3], v[56:57], 0, v[2:3]
	global_load_dwordx4 v[36:39], v[0:1], off
	global_load_dwordx4 v[40:43], v[2:3], off
	s_waitcnt vmcnt(2)
	v_mov_b64_e32 v[44:45], v[110:111]
	v_mov_b64_e32 v[46:47], v[112:113]
	v_mov_b64_e32 v[48:49], v[114:115]
	v_mov_b64_e32 v[50:51], v[116:117]
	v_mov_b32_e32 v74, v118
	v_mov_b32_e32 v76, v119
	v_mov_b64_e32 v[56:57], v[120:121]
	v_mov_b64_e32 v[58:59], v[122:123]
	v_mov_b64_e32 v[16:17], v[124:125]
	v_mov_b64_e32 v[18:19], v[126:127]
	v_or_b32_e32 v96, v104, v103
	s_add_i32 s3, s2, 0x3000
	s_lshr_b32 s4, s13, 4
	s_mov_b32 s7, 0
	s_mov_b64 s[0:1], -1
	s_mov_b32 s5, 0x7f61b1e6
	s_mov_b32 s6, 0x42800000
	s_waitcnt vmcnt(3)
	v_mov_b32_e32 v75, v74
	s_waitcnt vmcnt(2)
	v_mov_b32_e32 v77, v76
	s_nop 0
	s_branch .LBB2_10
.LBB2_9:
	s_waitcnt vmcnt(0)
	v_add_f32_e32 v1, v78, v79
	v_add_u32_e32 v0, s12, v97
	v_mul_f32_e32 v1, v74, v1
	v_lshl_or_b32 v2, v0, 3, s4
	v_exp_f32_e32 v4, v1
	v_mul_f32_e32 v5, v76, v66
	v_add_u32_e32 v0, s3, v2
	v_add_u32_e32 v2, s2, v2
	v_exp_f32_e32 v5, v5
	v_ashrrev_i32_e32 v3, 31, v2
	v_ashrrev_i32_e32 v1, 31, v0
	v_lshlrev_b64 v[2:3], 7, v[2:3]
	s_xor_b64 s[8:9], s[0:1], -1
	v_cvt_pk_f16_f32 v4, v4, v81
	v_lshl_add_u64 v[2:3], v[72:73], 0, v[2:3]
	v_lshlrev_b64 v[0:1], 7, v[0:1]
	v_mov_b64_e32 v[58:59], v[42:43]
	v_mov_b64_e32 v[16:17], v[36:37]
	global_store_dword v[2:3], v4, off
	v_cvt_pk_f16_f32 v2, v5, v67
	v_lshl_add_u64 v[0:1], v[72:73], 0, v[0:1]
	s_mov_b32 s7, 8
	s_mov_b64 s[0:1], 0
	s_andn2_b64 vcc, exec, s[8:9]
	v_mov_b64_e32 v[56:57], v[40:41]
	v_mov_b64_e32 v[18:19], v[38:39]
	global_store_dword v[0:1], v2, off
	s_cbranch_vccz .LBB2_15

	.amdhsa_kernel _Z11scan_kernelILi1ELi1536ELi4EEvPKfPKDF16_S3_S1_S1_PDv2_DF16_S3_Pf
		.amdhsa_group_segment_fixed_size 33280
		.amdhsa_private_segment_fixed_size 0
		.amdhsa_kernarg_size 64
		.amdhsa_user_sgpr_count 2
		.amdhsa_user_sgpr_dispatch_ptr 0
		.amdhsa_user_sgpr_queue_ptr 0
		.amdhsa_user_sgpr_kernarg_segment_ptr 1
		.amdhsa_user_sgpr_dispatch_id 0
		.amdhsa_user_sgpr_kernarg_preload_length 0
		.amdhsa_user_sgpr_kernarg_preload_offset 0
		.amdhsa_user_sgpr_private_segment_size 0
		.amdhsa_uses_dynamic_stack 0
		.amdhsa_enable_private_segment 0
		.amdhsa_system_sgpr_workgroup_id_x 1
		.amdhsa_system_sgpr_workgroup_id_y 0
		.amdhsa_system_sgpr_workgroup_id_z 0
		.amdhsa_system_sgpr_workgroup_info 0
		.amdhsa_system_vgpr_workitem_id 0
		.amdhsa_next_free_vgpr 128
		.amdhsa_next_free_sgpr 96
		.amdhsa_accum_offset 128
		.amdhsa_reserve_vcc 1
		.amdhsa_float_round_mode_32 0
		.amdhsa_float_round_mode_16_64 0
		.amdhsa_float_denorm_mode_32 3
		.amdhsa_float_denorm_mode_16_64 3
		.amdhsa_dx10_clamp 1
		.amdhsa_ieee_mode 1
		.amdhsa_fp16_overflow 0
		.amdhsa_tg_split 0
		.amdhsa_exception_fp_ieee_invalid_op 0
		.amdhsa_exception_fp_denorm_src 0
		.amdhsa_exception_fp_ieee_div_zero 0
		.amdhsa_exception_fp_ieee_overflow 0
		.amdhsa_exception_fp_ieee_underflow 0
		.amdhsa_exception_fp_ieee_inexact 0
		.amdhsa_exception_int_div_zero 0
	.end_amdhsa_kernel

amdhsa.kernels:
  - .agpr_count:     0
    .args:
      - .actual_access:  read_only
        .address_space:  global
        .offset:         0
        .size:           8
        .value_kind:     global_buffer
      - .actual_access:  read_only
        .address_space:  global
        .offset:         8
        .size:           8
        .value_kind:     global_buffer
      - .actual_access:  read_only
        .address_space:  global
        .offset:         16
        .size:           8
        .value_kind:     global_buffer
      - .actual_access:  read_only
        .address_space:  global
        .offset:         24
        .size:           8
        .value_kind:     global_buffer
      - .actual_access:  read_only
        .address_space:  global
        .offset:         32
        .size:           8
        .value_kind:     global_buffer
      - .actual_access:  read_only
        .address_space:  global
        .offset:         40
        .size:           8
        .value_kind:     global_buffer
      - .actual_access:  write_only
        .address_space:  global
        .offset:         48
        .size:           8
        .value_kind:     global_buffer
      - .actual_access:  write_only
        .address_space:  global
        .offset:         56
        .size:           8
        .value_kind:     global_buffer
      - .actual_access:  write_only
        .address_space:  global
        .offset:         64
        .size:           8
        .value_kind:     global_buffer
      - .actual_access:  write_only
        .address_space:  global
        .offset:         72
        .size:           8
        .value_kind:     global_buffer
    .group_segment_fixed_size: 65536
    .kernarg_segment_align: 8
    .kernarg_segment_size: 80
    .language:       OpenCL C
    .language_version:
      - 2
      - 0
    .max_flat_workgroup_size: 256
    .name:           _Z11proj_kernelPKfS0_S0_S0_S0_S0_PDF16_S1_PfS2_
    .private_segment_fixed_size: 0
    .sgpr_count:     22
    .sgpr_spill_count: 0
    .symbol:         _Z11proj_kernelPKfS0_S0_S0_S0_S0_PDF16_S1_PfS2_.kd
    .uniform_work_group_size: 1
    .uses_dynamic_stack: false
    .vgpr_count:     200
    .vgpr_spill_count: 0
    .wavefront_size: 64
  - .agpr_count:     0
    .args:
      - .actual_access:  read_only
        .address_space:  global
        .offset:         0
        .size:           8
        .value_kind:     global_buffer
      - .actual_access:  write_only
        .address_space:  global
        .offset:         8
        .size:           8
        .value_kind:     global_buffer
    .group_segment_fixed_size: 12672
    .kernarg_segment_align: 8
    .kernarg_segment_size: 16
    .language:       OpenCL C
    .language_version:
      - 2
      - 0
    .max_flat_workgroup_size: 1024
    .name:           _Z12carry_kernelPKDv2_DF16_PDF16_
    .private_segment_fixed_size: 0
    .sgpr_count:     16
    .sgpr_spill_count: 0
    .symbol:         _Z12carry_kernelPKDv2_DF16_PDF16_.kd
    .uniform_work_group_size: 1
    .uses_dynamic_stack: false
    .vgpr_count:     92
    .vgpr_spill_count: 0
    .wavefront_size: 64
  - .agpr_count:     0
    .args:
      - .actual_access:  read_only
        .address_space:  global
        .offset:         0
        .size:           8
        .value_kind:     global_buffer
      - .actual_access:  read_only
        .address_space:  global
        .offset:         8
        .size:           8
        .value_kind:     global_buffer
      - .actual_access:  read_only
        .address_space:  global
        .offset:         16
        .size:           8
        .value_kind:     global_buffer
      - .actual_access:  read_only
        .address_space:  global
        .offset:         24
        .size:           8
        .value_kind:     global_buffer
      - .actual_access:  read_only
        .address_space:  global
        .offset:         32
        .size:           8
        .value_kind:     global_buffer
      - .actual_access:  write_only
        .address_space:  global
        .offset:         40
        .size:           8
        .value_kind:     global_buffer
      - .actual_access:  read_only
        .address_space:  global
        .offset:         48
        .size:           8
        .value_kind:     global_buffer
      - .actual_access:  read_only
        .address_space:  global
        .offset:         56
        .size:           8
        .value_kind:     global_buffer
    .group_segment_fixed_size: 33280
    .kernarg_segment_align: 8
    .kernarg_segment_size: 64
    .language:       OpenCL C
    .language_version:
      - 2
      - 0
    .max_flat_workgroup_size: 256
    .name:           _Z11scan_kernelILi1ELi1536ELi4EEvPKfPKDF16_S3_S1_S1_PDv2_DF16_S3_Pf
    .private_segment_fixed_size: 0
    .sgpr_count:     24
    .sgpr_spill_count: 0
    .symbol:         _Z11scan_kernelILi1ELi1536ELi4EEvPKfPKDF16_S3_S1_S1_PDv2_DF16_S3_Pf.kd
    .uniform_work_group_size: 1
    .uses_dynamic_stack: false
    .vgpr_count:     128
    .vgpr_spill_count: 0
    .wavefront_size: 64
  - .agpr_count:     0
    .args:
      - .actual_access:  read_only
        .address_space:  global
        .offset:         0
        .size:           8
        .value_kind:     global_buffer
      - .actual_access:  read_only
        .address_space:  global
        .offset:         8
        .size:           8
        .value_kind:     global_buffer
      - .actual_access:  read_only
        .address_space:  global
        .offset:         16
        .size:           8
        .value_kind:     global_buffer
      - .actual_access:  read_only
        .address_space:  global
        .offset:         24
        .size:           8
        .value_kind:     global_buffer
      - .actual_access:  read_only
        .address_space:  global
        .offset:         32
        .size:           8
        .value_kind:     global_buffer
      - .actual_access:  read_only
        .address_space:  global
        .offset:         40
        .size:           8
        .value_kind:     global_buffer
      - .actual_access:  read_only
        .address_space:  global
        .offset:         48
        .size:           8
        .value_kind:     global_buffer
      - .actual_access:  write_only
        .address_space:  global
        .offset:         56
        .size:           8
        .value_kind:     global_buffer
    .group_segment_fixed_size: 50176
    .kernarg_segment_align: 8
    .kernarg_segment_size: 64
    .language:       OpenCL C
    .language_version:
      - 2
      - 0
    .max_flat_workgroup_size: 256
    .name:           _Z11scan_kernelILi3ELi1536ELi3EEvPKfPKDF16_S3_S1_S1_PDv2_DF16_S3_Pf
    .private_segment_fixed_size: 0
    .sgpr_count:     28
    .sgpr_spill_count: 0
    .symbol:         _Z11scan_kernelILi3ELi1536ELi3EEvPKfPKDF16_S3_S1_S1_PDv2_DF16_S3_Pf.kd
    .uniform_work_group_size: 1
    .uses_dynamic_stack: false
    .vgpr_count:     168
    .vgpr_spill_count: 0
    .wavefront_size: 64
